# router phases (both layers): per-bucket slot-reservation atomic issued at the histogram barrier so the ticket computation covers its round trip; on top of v61
# speedup vs baseline: 1.0068x; 1.0026x over previous
.LBB0_918:
	s_or_b64 exec, exec, s[16:17]
	s_waitcnt lgkmcnt(0)
	s_barrier
	s_and_saveexec_b64 s[12:13], s[6:7]
	v_lshl_add_u32 v70, v0, 2, 0
	v_add_u32_e32 v70, 0x1ed80, v70
	ds_read_b32 v71, v70
	v_mov_b32_e32 v72, 0
	v_lshlrev_b32_e32 v74, 7, v0
	v_add_u32_e32 v74, 0x10000, v74
	v_mov_b32_e32 v75, 0
	v_lshl_add_u64 v[74:75], s[54:55], 0, v[74:75]
	s_waitcnt lgkmcnt(0)
	v_cmp_ne_u32_e32 vcc, 0, v71
	s_and_b64 exec, exec, vcc
	global_atomic_add v72, v[74:75], v71, off sc0
	s_or_b64 exec, exec, s[12:13]
	s_and_saveexec_b64 s[10:11], s[8:9]
	s_cbranch_execz .LBB0_936
	v_lshl_add_u32 v4, v0, 2, 0
	v_add_u32_e32 v1, 0x1efc0, v4
	ds_read_b32 v3, v1
	v_mov_b32_e32 v1, 0
	s_mov_b64 s[12:13], exec
	v_readlane_b32 s8, v253, 34
	v_readlane_b32 s9, v253, 35
	s_and_b64 s[8:9], s[12:13], s[8:9]
	s_mov_b64 exec, s[8:9]
	s_cbranch_execz .LBB0_935
	v_cmp_ne_u32_e32 vcc, 1, v0
	s_mov_b64 s[16:17], -1
	v_mov_b32_e32 v1, 0
	v_mov_b32_e32 v5, 0
	s_and_saveexec_b64 s[14:15], vcc
	s_cbranch_execz .LBB0_930
	v_add_u32_e32 v1, -2, v0
	v_lshrrev_b32_e32 v2, 1, v1
	v_add_u32_e32 v5, 1, v2
	v_mov_b32_e32 v2, 0
	v_cmp_lt_u32_e32 vcc, 13, v1
	s_mov_b32 s20, 0
	v_mov_b32_e32 v1, v2
	v_mov_b32_e32 v7, v2
	s_and_saveexec_b64 s[16:17], vcc
	s_cbranch_execz .LBB0_925
	s_add_i32 s21, 0, 0x1efc0
	v_and_b32_e32 v6, -8, v5
	s_mov_b64 s[18:19], 0
	v_mov_b32_e32 v2, 0
	v_mov_b32_e32 v1, 0

.LBB0_936:
	s_or_b64 exec, exec, s[10:11]
	s_waitcnt lgkmcnt(0)
	s_barrier
	s_and_saveexec_b64 s[8:9], s[6:7]
	s_cbranch_execz .LBB0_940
	v_lshl_add_u32 v1, v0, 2, 0
	v_add_u32_e32 v1, 0x1ee00, v1
	s_waitcnt vmcnt(0)
	ds_write_b32 v1, v72

.LBB0_1965:
	s_or_b64 exec, exec, s[14:15]
	s_waitcnt lgkmcnt(0)
	s_barrier
	s_and_saveexec_b64 s[2:3], s[6:7]
	v_lshl_add_u32 v70, v0, 2, 0
	v_add_u32_e32 v70, 0x1ed80, v70
	ds_read_b32 v71, v70
	v_mov_b32_e32 v72, 0
	v_lshlrev_b32_e32 v74, 7, v0
	v_add_u32_e32 v74, 0x11000, v74
	v_mov_b32_e32 v75, 0
	v_lshl_add_u64 v[74:75], s[50:51], 0, v[74:75]
	s_waitcnt lgkmcnt(0)
	v_cmp_ne_u32_e32 vcc, 0, v71
	s_and_b64 exec, exec, vcc
	global_atomic_add v72, v[74:75], v71, off sc0
	s_or_b64 exec, exec, s[2:3]
	s_and_saveexec_b64 s[10:11], s[8:9]
	s_cbranch_execz .LBB0_1983
	v_lshl_add_u32 v4, v0, 2, 0
	v_add_u32_e32 v1, 0x1efc0, v4
	ds_read_b32 v3, v1
	v_mov_b32_e32 v1, 0
	s_mov_b64 s[8:9], exec
	v_readlane_b32 s2, v253, 34
	v_readlane_b32 s3, v253, 35
	s_and_b64 s[2:3], s[8:9], s[2:3]
	s_mov_b64 exec, s[2:3]
	s_cbranch_execz .LBB0_1982
	v_cmp_ne_u32_e32 vcc, 1, v0
	s_mov_b64 s[14:15], -1
	v_mov_b32_e32 v1, 0
	v_mov_b32_e32 v5, 0
	s_and_saveexec_b64 s[12:13], vcc
	s_cbranch_execz .LBB0_1977
	v_add_u32_e32 v1, -2, v0
	v_lshrrev_b32_e32 v2, 1, v1
	v_add_u32_e32 v5, 1, v2
	v_mov_b32_e32 v2, 0
	v_cmp_lt_u32_e32 vcc, 13, v1
	s_mov_b32 s18, 0
	v_mov_b32_e32 v1, v2
	v_mov_b32_e32 v7, v2
	s_and_saveexec_b64 s[14:15], vcc
	s_cbranch_execz .LBB0_1972
	s_add_i32 s19, 0, 0x1efc0
	v_and_b32_e32 v6, -8, v5
	s_mov_b64 s[16:17], 0
	v_mov_b32_e32 v2, 0
	v_mov_b32_e32 v1, 0

.LBB0_1983:
	s_or_b64 exec, exec, s[10:11]
	s_waitcnt lgkmcnt(0)
	s_barrier
	s_and_saveexec_b64 s[2:3], s[6:7]
	s_cbranch_execz .LBB0_1987
	v_lshl_add_u32 v1, v0, 2, 0
	v_add_u32_e32 v1, 0x1ee00, v1
	s_waitcnt vmcnt(0)
	ds_write_b32 v1, v72
